# conv WGs in P1 paced with s_sleep 48 per item to reduce memory contention against the in-proj GEMM
# speedup vs baseline: 1.0016x; 1.0016x over previous
; #define LAS __attribute__((address_space(3)))
; #define CONV_LOAD(dst, ci, half) do { const float* src_ = (ci).W + (size_t)((ci).k0 + 64 * (half) + 4 * kq) * 2048 + (ci).n0 + 4 * nq; \
;         _Pragma("unroll") for (int i_ = 0; i_ < 4; ++i_) _Pragma("unroll") for (int j_ = 0; j_ < 4; ++j_) dst[i_][j_] = __builtin_nontemporal_load((const f32x4*)(src_ + (size_t)(16 * i_ + j_) * 2048)); } while (0)
; __device__ __forceinline__ void moe_weight_convert(const Params& p, Frame& F, int gw, int NGW, int it0, int NIT) {
;     LAS unsigned char* tile = F.lds + 16384 + F.wave * 8192;
;     const int lane = F.lane, kq = lane >> 4, nq = lane & 15;
;     __syncthreads();
;     for (int i = F.tid; i < DM; i += 512) { *(LAS float*)(F.lds + 4 * i) = p.in[11][i] * 64.0f; *(LAS float*)(F.lds + 8192 + 4 * i) = 64.0f; }
;     __syncthreads();
;     int it = it0 + gw; if (it >= NIT) return;
;     ConvItem cur = conv_item(p, it);
;     f32x4 va[4][4], vb[4][4];
;     CONV_LOAD(va, cur, 0);
;     for (;;) {
;         CONV_LOAD(vb, cur, 1);
;         CONV_PACK(va, cur, 0);
;         const int nit = it + NGW; const bool more = nit < NIT;
;         const ConvItem nxt = conv_item(p, more ? nit : it);
;         CONV_LOAD(va, nxt, 0);
;         CONV_PACK(vb, cur, 1);
;         CONV_STORE(cur);
;         if (!more) break;
;         cur = nxt; it = nit;
;     }
.LBB0_165:
	s_sleep 48
	v_or_b32_e32 v64, s36, v1
	v_or_b32_e32 v134, 64, v64
	v_ashrrev_i32_e32 v135, 31, v134
	v_lshlrev_b64 v[34:35], 13, v[134:135]
	v_lshl_add_u64 v[34:35], s[6:7], 0, v[34:35]
	s_ashr_i32 s5, s4, 31
	v_lshl_add_u64 v[34:35], s[4:5], 2, v[34:35]
	v_lshl_add_u64 v[106:107], v[34:35], 0, v[130:131]
	v_add_co_u32_e32 v34, vcc, s23, v106
	s_add_i32 s47, s16, 0
	s_nop 0
	v_addc_co_u32_e32 v35, vcc, 0, v107, vcc
	global_load_dwordx4 v[82:85], v[106:107], off nt
	global_load_dwordx4 v[86:89], v[34:35], off nt
	v_add_co_u32_e32 v34, vcc, s24, v106
	v_lshl_add_u32 v135, v64, 2, s47
	s_nop 0
	v_addc_co_u32_e32 v35, vcc, 0, v107, vcc
	v_add_co_u32_e32 v36, vcc, s25, v106
	v_mov_b32_e32 v78, v131
	s_nop 0
	v_addc_co_u32_e32 v37, vcc, 0, v107, vcc
	global_load_dwordx4 v[90:93], v[34:35], off nt
	global_load_dwordx4 v[94:97], v[36:37], off nt
	v_add_co_u32_e32 v34, vcc, s26, v106
	v_mov_b32_e32 v79, v131
	s_nop 0
	v_addc_co_u32_e32 v35, vcc, 0, v107, vcc
	v_add_co_u32_e32 v36, vcc, s27, v106
	s_add_i32 s4, s44, s45
	s_nop 0
	v_addc_co_u32_e32 v37, vcc, 0, v107, vcc
	global_load_dwordx4 v[50:53], v[34:35], off nt
	global_load_dwordx4 v[54:57], v[36:37], off nt
	v_add_co_u32_e32 v34, vcc, s28, v106
	s_add_i32 s5, s46, s45
	s_nop 0
	v_addc_co_u32_e32 v35, vcc, 0, v107, vcc
	v_add_co_u32_e32 v36, vcc, s29, v106
	s_cmp_lt_i32 s5, 0x8000
	s_nop 0
	v_addc_co_u32_e32 v37, vcc, 0, v107, vcc
	global_load_dwordx4 v[58:61], v[34:35], off nt
	global_load_dwordx4 v[70:73], v[36:37], off nt
	v_add_co_u32_e32 v34, vcc, s30, v106
	s_cselect_b32 s11, s5, s4
	s_nop 0
	v_addc_co_u32_e32 v35, vcc, 0, v107, vcc
	v_add_co_u32_e32 v38, vcc, s31, v106
	s_cmpk_gt_i32 s11, 0x7fff
	s_nop 0
	v_addc_co_u32_e32 v39, vcc, 0, v107, vcc
	global_load_dwordx4 v[34:37], v[34:35], off nt
	s_nop 0
	global_load_dwordx4 v[38:41], v[38:39], off nt
	ds_read_b128 v[74:77], v135
	v_add_co_u32_e32 v62, vcc, s33, v106
	s_cselect_b64 s[4:5], -1, 0
	s_nop 0
	v_addc_co_u32_e32 v63, vcc, 0, v107, vcc
	s_waitcnt vmcnt(25) lgkmcnt(0)
	v_mul_f32_e32 v6, v6, v74
	s_waitcnt vmcnt(24)
	v_mul_f32_e32 v14, v14, v75
	v_cvt_pk_fp8_f32 v78, v6, v14
	v_mul_f32_e32 v6, v7, v74
	v_mul_f32_e32 v7, v15, v75
	v_cvt_pk_fp8_f32 v79, v6, v7
	s_waitcnt vmcnt(23)
	v_mul_f32_e32 v6, v23, v76
	s_waitcnt vmcnt(22)
	v_mul_f32_e32 v7, v31, v77
	v_mul_f32_e32 v22, v22, v76
	v_cvt_pk_fp8_f32 v79, v6, v7 op_sel:[0,0,1]
	v_mul_f32_e32 v6, v8, v74
	v_mul_f32_e32 v7, v16, v75
	v_mov_b32_e32 v16, v131
	v_cvt_pk_fp8_f32 v16, v6, v7
	v_mul_f32_e32 v6, v9, v74
	v_mul_f32_e32 v7, v17, v75
	v_mov_b32_e32 v9, v131
	v_cvt_pk_fp8_f32 v9, v6, v7
	v_mul_f32_e32 v30, v30, v77
	v_cvt_pk_fp8_f32 v78, v22, v30 op_sel:[0,0,1]
	v_mul_f32_e32 v8, v24, v76
	v_mul_f32_e32 v14, v32, v77
	v_mul_f32_e32 v6, v25, v76
	v_mul_f32_e32 v7, v33, v77
	v_cvt_pk_fp8_f32 v16, v8, v14 op_sel:[0,0,1]
	v_cvt_pk_fp8_f32 v9, v6, v7 op_sel:[0,0,1]
	v_add_co_u32_e32 v66, vcc, s34, v106
	v_add_u32_e32 v6, 0x4000, v144
	s_nop 0
	v_addc_co_u32_e32 v67, vcc, 0, v107, vcc
	global_load_dwordx4 v[62:65], v[62:63], off nt
	s_nop 0
	global_load_dwordx4 v[66:69], v[66:67], off nt
	ds_write2_b32 v6, v78, v79 offset1:32
	ds_write2_b32 v6, v16, v9 offset0:64 offset1:96
	ds_read_b128 v[6:9], v135 offset:64
	v_add_co_u32_e32 v14, vcc, s35, v106
	s_cmp_lt_i32 s11, 0x8000
	s_nop 0
	v_addc_co_u32_e32 v15, vcc, 0, v107, vcc
	v_add_co_u32_e32 v16, vcc, s37, v106
	s_waitcnt vmcnt(23) lgkmcnt(0)
	v_mul_f32_e32 v2, v2, v6
	v_addc_co_u32_e32 v17, vcc, 0, v107, vcc
	global_load_dwordx4 v[74:77], v[14:15], off nt
	global_load_dwordx4 v[78:81], v[16:17], off nt
	s_waitcnt vmcnt(24)
; #define CONV_LOAD(dst, ci, half) do { const float* src_ = (ci).W + (size_t)((ci).k0 + 64 * (half) + 4 * kq) * 2048 + (ci).n0 + 4 * nq; \
;         _Pragma("unroll") for (int i_ = 0; i_ < 4; ++i_) _Pragma("unroll") for (int j_ = 0; j_ < 4; ++j_) dst[i_][j_] = __builtin_nontemporal_load((const f32x4*)(src_ + (size_t)(16 * i_ + j_) * 2048)); } while (0)
; __device__ __forceinline__ void moe_weight_convert(const Params& p, Frame& F, int gw, int NGW, int it0, int NIT) {
;     ...
;         const int nit = it + NGW; const bool more = nit < NIT;
;         const ConvItem nxt = conv_item(p, more ? nit : it);
;         CONV_LOAD(va, nxt, 0);
;         CONV_PACK(vb, cur, 1);
	v_mul_f32_e32 v10, v10, v7
	v_mov_b32_e32 v16, v131
	v_cvt_pk_fp8_f32 v16, v2, v10
	v_mul_f32_e32 v2, v3, v6
	v_mul_f32_e32 v3, v11, v7
	v_mov_b32_e32 v10, v131
	v_cvt_pk_fp8_f32 v10, v2, v3
	s_waitcnt vmcnt(23)
	v_mul_f32_e32 v2, v19, v8
	s_waitcnt vmcnt(22)
	v_mul_f32_e32 v3, v27, v9
	v_mul_f32_e32 v14, v18, v8
	v_cvt_pk_fp8_f32 v10, v2, v3 op_sel:[0,0,1]
	v_mul_f32_e32 v2, v4, v6
	v_mul_f32_e32 v3, v12, v7
	v_mov_b32_e32 v12, v131
	v_cvt_pk_fp8_f32 v12, v2, v3
	v_mul_f32_e32 v2, v5, v6
	v_mul_f32_e32 v3, v13, v7
	v_mov_b32_e32 v5, v131
	v_cvt_pk_fp8_f32 v5, v2, v3
	v_mul_f32_e32 v15, v26, v9
	v_cvt_pk_fp8_f32 v16, v14, v15 op_sel:[0,0,1]
	v_mul_f32_e32 v4, v20, v8
	v_mul_f32_e32 v11, v28, v9
	v_mul_f32_e32 v2, v21, v8
	v_mul_f32_e32 v3, v29, v9
	v_cvt_pk_fp8_f32 v12, v4, v11 op_sel:[0,0,1]
	v_cvt_pk_fp8_f32 v5, v2, v3 op_sel:[0,0,1]
	v_add_co_u32_e32 v6, vcc, s38, v106
	v_add_u32_e32 v2, 0x4000, v145
	s_nop 0
	v_addc_co_u32_e32 v7, vcc, 0, v107, vcc
	ds_write2_b32 v2, v16, v10 offset1:32
	ds_write2_b32 v2, v12, v5 offset0:64 offset1:96
	v_add_co_u32_e32 v8, vcc, s39, v106
	ds_read_b128 v[2:5], v135 offset:128
	s_nop 0
	v_addc_co_u32_e32 v9, vcc, 0, v107, vcc
	global_load_dwordx4 v[106:109], v[6:7], off nt
	global_load_dwordx4 v[110:113], v[8:9], off nt
	v_mov_b32_e32 v10, v131
	s_waitcnt vmcnt(23) lgkmcnt(0)
	v_mul_f32_e32 v6, v42, v2
	s_waitcnt vmcnt(22)
	v_mul_f32_e32 v7, v46, v3
	v_cvt_pk_fp8_f32 v10, v6, v7
	v_mul_f32_e32 v6, v43, v2
	v_mul_f32_e32 v7, v47, v3
	v_mov_b32_e32 v11, v131
	v_cvt_pk_fp8_f32 v11, v6, v7
	s_waitcnt vmcnt(21)
	v_mul_f32_e32 v6, v99, v4
	s_waitcnt vmcnt(20)
	v_mul_f32_e32 v7, v103, v5
	v_mov_b32_e32 v12, v131
	v_cvt_pk_fp8_f32 v11, v6, v7 op_sel:[0,0,1]
	v_mul_f32_e32 v6, v44, v2
	v_mul_f32_e32 v7, v48, v3
	v_cvt_pk_fp8_f32 v12, v6, v7
	v_mul_f32_e32 v2, v45, v2
	v_mul_f32_e32 v3, v49, v3
	v_mov_b32_e32 v6, v131
	v_cvt_pk_fp8_f32 v6, v2, v3
	v_mul_f32_e32 v8, v98, v4
	v_mul_f32_e32 v9, v102, v5
	v_cvt_pk_fp8_f32 v10, v8, v9 op_sel:[0,0,1]
	v_mul_f32_e32 v8, v100, v4
	v_mul_f32_e32 v9, v104, v5
	v_mul_f32_e32 v2, v101, v4
	v_mul_f32_e32 v3, v105, v5
	v_cvt_pk_fp8_f32 v12, v8, v9 op_sel:[0,0,1]
	v_cvt_pk_fp8_f32 v6, v2, v3 op_sel:[0,0,1]
	v_add_u32_e32 v2, 0x4000, v146
	ds_write2_b32 v2, v10, v11 offset1:32
	ds_write2_b32 v2, v12, v6 offset0:64 offset1:96
	ds_read_b128 v[2:5], v135 offset:192
	v_mov_b32_e32 v10, v131
	v_mov_b32_e32 v11, v131
	v_mov_b32_e32 v12, v131
	s_cselect_b64 s[6:7], -1, 0
	s_waitcnt vmcnt(19) lgkmcnt(0)
	v_mul_f32_e32 v6, v114, v2
	s_waitcnt vmcnt(18)
	v_mul_f32_e32 v7, v118, v3
	v_cvt_pk_fp8_f32 v10, v6, v7
	v_mul_f32_e32 v6, v115, v2
	v_mul_f32_e32 v7, v119, v3
	v_cvt_pk_fp8_f32 v11, v6, v7
	s_waitcnt vmcnt(17)
	v_mul_f32_e32 v6, v123, v4
	s_waitcnt vmcnt(16)
	v_mul_f32_e32 v7, v127, v5
	v_mul_f32_e32 v8, v122, v4
	v_cvt_pk_fp8_f32 v11, v6, v7 op_sel:[0,0,1]
	v_mul_f32_e32 v6, v116, v2
	v_mul_f32_e32 v7, v120, v3
	v_cvt_pk_fp8_f32 v12, v6, v7
	v_mul_f32_e32 v2, v117, v2
	v_mul_f32_e32 v3, v121, v3
	v_mov_b32_e32 v6, v131
	v_cvt_pk_fp8_f32 v6, v2, v3
	v_mul_f32_e32 v9, v126, v5
	v_cvt_pk_fp8_f32 v10, v8, v9 op_sel:[0,0,1]
	v_mul_f32_e32 v8, v124, v4
	v_mul_f32_e32 v9, v128, v5
	v_mul_f32_e32 v2, v125, v4
	v_mul_f32_e32 v3, v129, v5
	v_cvt_pk_fp8_f32 v12, v8, v9 op_sel:[0,0,1]
	v_cvt_pk_fp8_f32 v6, v2, v3 op_sel:[0,0,1]
	v_add_u32_e32 v2, 0x4000, v147
	s_mov_b64 s[8:9], -1
	s_and_b64 vcc, exec, s[6:7]
	ds_write2_b32 v2, v10, v11 offset1:32
	ds_write2_b32 v2, v12, v6 offset0:64 offset1:96
	s_cbranch_vccnz .LBB0_173
	s_andn2_b64 vcc, exec, s[8:9]
	s_add_i32 s8, s11, 0xffff8000
	s_cbranch_vccz .LBB0_174
